# speedup vs baseline: 1.0094x; 1.0004x over previous
_Z11main_kernelPKfPKiPK15HIP_vector_typeIjLj4EES0_PfS7_S2_i:
	v_and_b32_e32 v104, 0x3ff, v0
	s_mul_i32 s2, s2, 12
	v_readfirstlane_b32 s3, v104
	s_lshr_b32 s3, s3, 6
	s_add_i32 s2, s3, s2
	s_load_dwordx8 s[12:19], s[0:1], 0x0
	s_load_dwordx2 s[10:11], s[0:1], 0x30
	s_mul_i32 s2, s2, 0xf424
	s_mul_hi_u32 s4, s2, 0xaaaaaaab
	s_add_i32 s2, s2, 0xf424
	s_mul_hi_u32 s2, s2, 0xaaaaaaab
	s_lshr_b32 s42, s2, 11
	s_lshl_b32 s2, s3, 8
	v_and_b32_e32 v1, 15, v0
	v_bfe_u32 v112, v0, 4, 2
	s_lshr_b32 s44, s4, 11
	s_lshl_b32 s33, s3, 13
	s_add_i32 s43, s2, 0x20000
	s_cmp_lt_u32 s33, 0x8000
	s_cbranch_scc1 .Lmain_older
	s_setprio 1
